# v24 + waves 0-3: P.V MFMAs of sub-head 0, key-step 0, moved from the end-of-tile P.V pass into the gap after the sub-head-0 softmax (replacing the idle spacer)
# baseline (speedup 1.0000x reference)
.LBB0_205:
	v_add_u32_e32 v219, v212, v232
	v_add_u32_e32 v212, v212, v233
	s_waitcnt lgkmcnt(0)
	v_mfma_f32_32x32x16_bf16 v[144:159], v[248:251], v[192:195], v[144:159]
	ds_read_b128 v[248:251], v219
	v_mfma_f32_32x32x16_bf16 v[160:175], v[236:239], v[192:195], v[160:175]
	ds_read_b128 v[236:239], v219 offset:8192
	v_mfma_f32_32x32x16_bf16 v[144:159], v[240:243], v[196:199], v[144:159]
	ds_read_b128 v[240:243], v212
	v_mfma_f32_32x32x16_bf16 v[160:175], v[244:247], v[196:199], v[160:175]
	ds_read_b128 v[244:247], v212 offset:8192
	s_waitcnt lgkmcnt(3)
	v_mfma_f32_32x32x16_bf16 v[144:159], v[248:251], v[200:203], v[144:159]
	s_waitcnt lgkmcnt(2)
	v_mfma_f32_32x32x16_bf16 v[160:175], v[236:239], v[200:203], v[160:175]
	v_add_f32_e32 v212, v213, v218
	v_add_f32_e32 v235, v235, v212
	s_waitcnt lgkmcnt(1)
	v_mfma_f32_32x32x16_bf16 v[144:159], v[240:243], v[204:207], v[144:159]
	s_waitcnt lgkmcnt(0)
	v_mfma_f32_32x32x16_bf16 v[160:175], v[244:247], v[204:207], v[160:175]
	s_nop 10
	v_exp_f32_e32 v212, v144
	v_exp_f32_e32 v218, v145
	v_exp_f32_e32 v242, v148
	v_exp_f32_e32 v244, v149
	v_exp_f32_e32 v213, v152
	v_exp_f32_e32 v219, v153
	v_exp_f32_e32 v243, v156
	v_exp_f32_e32 v245, v157
	v_exp_f32_e32 v236, v146
	v_exp_f32_e32 v150, v150
	v_exp_f32_e32 v248, v151
	v_exp_f32_e32 v237, v154
	v_exp_f32_e32 v151, v158
	v_exp_f32_e32 v238, v147
	v_exp_f32_e32 v239, v155
	v_exp_f32_e32 v249, v159
	v_exp_f32_e32 v160, v160
	v_exp_f32_e32 v220, v161
	v_exp_f32_e32 v164, v164
	v_exp_f32_e32 v246, v165
	v_exp_f32_e32 v161, v168
	v_exp_f32_e32 v165, v172
	v_exp_f32_e32 v221, v169
	v_exp_f32_e32 v247, v173
	v_pk_add_f32 v[144:145], v[212:213], v[218:219]
	v_pk_add_f32 v[146:147], v[242:243], v[244:245]
	v_exp_f32_e32 v162, v162
	v_exp_f32_e32 v240, v163
	v_exp_f32_e32 v166, v166
	v_exp_f32_e32 v250, v167
	v_exp_f32_e32 v163, v170
	v_exp_f32_e32 v167, v174
	v_pk_add_f32 v[144:145], v[236:237], v[144:145]
	v_pk_add_f32 v[146:147], v[150:151], v[146:147]
	v_exp_f32_e32 v241, v171
	v_exp_f32_e32 v251, v175
	v_pk_add_f32 v[144:145], v[238:239], v[144:145]
	v_pk_add_f32 v[146:147], v[248:249], v[146:147]
	v_pk_add_f32 v[144:145], v[160:161], v[144:145]
	v_pk_add_f32 v[146:147], v[164:165], v[146:147]
	v_pk_add_f32 v[144:145], v[220:221], v[144:145]
	v_pk_add_f32 v[146:147], v[246:247], v[146:147]
	v_pk_add_f32 v[144:145], v[162:163], v[144:145]
	v_pk_add_f32 v[146:147], v[166:167], v[146:147]
	v_pk_add_f32 v[144:145], v[240:241], v[144:145]
	v_pk_add_f32 v[146:147], v[250:251], v[146:147]
	v_cvt_pk_bf16_f32 v148, v213, v219
	v_pk_add_f32 v[144:145], v[144:145], v[146:147]
	v_cvt_pk_bf16_f32 v146, v242, v244
	v_pk_add_f32 v[144:145], v[144:145], v[144:145] op_sel:[0,1] op_sel_hi:[1,0]
	v_cvt_pk_bf16_f32 v147, v150, v248
	v_mov_b32_e32 v145, v144
	s_nop 1
	v_permlane32_swap_b32_e32 v144, v145
	v_add_f32_e32 v144, v144, v145
	v_add_f32_e32 v234, v234, v144
	v_cvt_pk_bf16_f32 v144, v212, v218
	v_cvt_pk_bf16_f32 v145, v236, v238
	v_cvt_pk_bf16_f32 v149, v237, v239
	v_cvt_pk_bf16_f32 v150, v243, v245
	v_cvt_pk_bf16_f32 v151, v151, v249
	v_cvt_pk_bf16_f32 v152, v160, v220
	v_cvt_pk_bf16_f32 v153, v162, v240
	v_cvt_pk_bf16_f32 v154, v164, v246
	v_cvt_pk_bf16_f32 v155, v166, v250
	v_cvt_pk_bf16_f32 v156, v161, v221
	v_cvt_pk_bf16_f32 v157, v163, v241
	v_cvt_pk_bf16_f32 v158, v165, v247
	v_cvt_pk_bf16_f32 v159, v167, v251
	v_permlane32_swap_b32_e32 v144, v146
	v_permlane32_swap_b32_e32 v145, v147
	v_permlane32_swap_b32_e32 v148, v150
	v_permlane32_swap_b32_e32 v149, v151
	v_permlane32_swap_b32_e32 v152, v154
	v_permlane32_swap_b32_e32 v153, v155
	v_permlane32_swap_b32_e32 v156, v158
	v_permlane32_swap_b32_e32 v157, v159
	s_waitcnt lgkmcnt(0)
	v_add_u32_e32 v212, s56, v224
	ds_read_b64_tr_b16 v[160:161], v212 offset:0
	ds_read_b64_tr_b16 v[162:163], v212 offset:0x800
	ds_read_b64_tr_b16 v[164:165], v212 offset:0x200
	ds_read_b64_tr_b16 v[166:167], v212 offset:0xa00
	ds_read_b64_tr_b16 v[168:169], v212 offset:0x400
	ds_read_b64_tr_b16 v[170:171], v212 offset:0xc00
	ds_read_b64_tr_b16 v[172:173], v212 offset:0x600
	ds_read_b64_tr_b16 v[174:175], v212 offset:0xe00
	s_waitcnt lgkmcnt(4)
	s_nop 0
	v_mfma_f32_32x32x16_bf16 v[128:143], v[144:147], v[160:163], v[128:143]
	v_mfma_f32_32x32x16_bf16 v[80:95], v[144:147], v[164:167], v[80:95]
	ds_read_b64_tr_b16 v[160:161], v212 offset:0x1000
	ds_read_b64_tr_b16 v[162:163], v212 offset:0x1800
	ds_read_b64_tr_b16 v[164:165], v212 offset:0x1200
	ds_read_b64_tr_b16 v[166:167], v212 offset:0x1a00
	s_waitcnt lgkmcnt(4)
	v_mfma_f32_32x32x16_bf16 v[32:47], v[144:147], v[168:171], v[32:47]
	v_mfma_f32_32x32x16_bf16 v[16:31], v[144:147], v[172:175], v[16:31]
	ds_read_b64_tr_b16 v[144:145], v212 offset:0x1400
	ds_read_b64_tr_b16 v[146:147], v212 offset:0x1c00
	ds_read_b64_tr_b16 v[168:169], v212 offset:0x1600
	ds_read_b64_tr_b16 v[170:171], v212 offset:0x1e00
	s_waitcnt lgkmcnt(4)
	v_mfma_f32_32x32x16_bf16 v[112:127], v[10:13], v[160:163], v[112:127]
	v_mfma_f32_32x32x16_bf16 v[96:111], v[10:13], v[164:167], v[96:111]
	v_mfma_f32_32x32x16_bf16 v[128:143], v[148:151], v[160:163], v[128:143]
	v_mfma_f32_32x32x16_bf16 v[80:95], v[148:151], v[164:167], v[80:95]
	ds_read_b64_tr_b16 v[160:161], v212 offset:0x2000
	ds_read_b64_tr_b16 v[162:163], v212 offset:0x2800
	ds_read_b64_tr_b16 v[164:165], v212 offset:0x2200
	ds_read_b64_tr_b16 v[166:167], v212 offset:0x2a00
	s_waitcnt lgkmcnt(4)
	v_mfma_f32_32x32x16_bf16 v[64:79], v[10:13], v[144:147], v[64:79]
	v_mfma_f32_32x32x16_bf16 v[48:63], v[10:13], v[168:171], v[48:63]
	v_mfma_f32_32x32x16_bf16 v[32:47], v[148:151], v[144:147], v[32:47]
	v_mfma_f32_32x32x16_bf16 v[16:31], v[148:151], v[168:171], v[16:31]
	ds_read_b64_tr_b16 v[10:11], v212 offset:0x2400
	ds_read_b64_tr_b16 v[12:13], v212 offset:0x2c00
	ds_read_b64_tr_b16 v[144:145], v212 offset:0x2600
	ds_read_b64_tr_b16 v[146:147], v212 offset:0x2e00
	s_waitcnt lgkmcnt(4)
	v_mfma_f32_32x32x16_bf16 v[112:127], v[6:9], v[160:163], v[112:127]
	v_mfma_f32_32x32x16_bf16 v[96:111], v[6:9], v[164:167], v[96:111]
	v_mfma_f32_32x32x16_bf16 v[128:143], v[152:155], v[160:163], v[128:143]
	v_mfma_f32_32x32x16_bf16 v[80:95], v[152:155], v[164:167], v[80:95]
	ds_read_b64_tr_b16 v[148:149], v212 offset:0x3000
	ds_read_b64_tr_b16 v[150:151], v212 offset:0x3800
	ds_read_b64_tr_b16 v[160:161], v212 offset:0x3200
	ds_read_b64_tr_b16 v[162:163], v212 offset:0x3a00
	s_waitcnt lgkmcnt(4)
	v_mfma_f32_32x32x16_bf16 v[64:79], v[6:9], v[10:13], v[64:79]
	v_mfma_f32_32x32x16_bf16 v[48:63], v[6:9], v[144:147], v[48:63]
	v_mfma_f32_32x32x16_bf16 v[32:47], v[152:155], v[10:13], v[32:47]
	v_mfma_f32_32x32x16_bf16 v[16:31], v[152:155], v[144:147], v[16:31]
	ds_read_b64_tr_b16 v[6:7], v212 offset:0x3400
	ds_read_b64_tr_b16 v[8:9], v212 offset:0x3c00
	ds_read_b64_tr_b16 v[10:11], v212 offset:0x3600
	ds_read_b64_tr_b16 v[12:13], v212 offset:0x3e00
	s_waitcnt lgkmcnt(4)
	v_mfma_f32_32x32x16_bf16 v[112:127], v[2:5], v[148:151], v[112:127]
	v_mfma_f32_32x32x16_bf16 v[96:111], v[2:5], v[160:163], v[96:111]
	v_mfma_f32_32x32x16_bf16 v[128:143], v[156:159], v[148:151], v[128:143]
	v_mfma_f32_32x32x16_bf16 v[80:95], v[156:159], v[160:163], v[80:95]
	s_waitcnt lgkmcnt(0)
	v_mfma_f32_32x32x16_bf16 v[64:79], v[2:5], v[6:9], v[64:79]
	v_mfma_f32_32x32x16_bf16 v[48:63], v[2:5], v[10:13], v[48:63]
	v_mfma_f32_32x32x16_bf16 v[32:47], v[156:159], v[6:9], v[32:47]
	v_mfma_f32_32x32x16_bf16 v[16:31], v[156:159], v[10:13], v[16:31]
	s_add_i32 s42, s56, 0x4000
	s_cmpk_lg_u32 s56, 0xc000
	s_cselect_b32 s56, s42, 0
	s_add_i32 s42, s90, 0x4000
	s_cmpk_lg_u32 s90, 0xc000
	s_cselect_b32 s90, s42, 0
	s_add_u32 s40, s40, 0x60000
	s_addc_u32 s41, s41, 0
	s_addk_i32 s73, 0x100
	s_add_i32 s72, s72, 64
	s_add_i32 s71, s71, 1
	s_cmpk_eq_i32 s73, 0x4000
	s_cbranch_scc1 .LBB0_220

.LBB0_215:
	v_add_u32_e32 v212, s56, v225
	v_add_u32_e32 v6, v212, v227
	v_add_u32_e32 v7, v212, v228
	ds_read_b128 v[244:247], v6
	ds_read_b128 v[248:251], v6 offset:8192
	ds_read_b128 v[236:239], v7
	ds_read_b128 v[240:243], v7 offset:8192
	v_add_u32_e32 v6, v212, v229
	v_add_u32_e32 v7, v212, v230
	ds_read_b128 v[2:5], v6
	ds_read_b128 v[8:11], v6 offset:8192
	ds_read_b128 v[208:211], v7
	s_xor_b64 s[44:45], s[44:45], -1
	v_add_u32_e32 v6, v212, v226
	s_waitcnt lgkmcnt(6)
	v_mfma_f32_32x32x16_bf16 v[160:175], v[244:247], v[176:179], v[160:175]
	ds_read_b128 v[244:247], v7 offset:8192
	s_waitcnt lgkmcnt(6)
	v_mfma_f32_32x32x16_bf16 v[144:159], v[248:251], v[176:179], v[144:159]
	s_waitcnt lgkmcnt(5)
	v_mfma_f32_32x32x16_bf16 v[160:175], v[236:239], v[180:183], v[160:175]
	v_add_u32_e32 v7, v212, v231
	s_waitcnt lgkmcnt(4)
	v_mfma_f32_32x32x16_bf16 v[144:159], v[240:243], v[180:183], v[144:159]
	ds_read_b128 v[248:251], v6
	ds_read_b128 v[236:239], v6 offset:8192
	ds_read_b128 v[240:243], v7
	s_waitcnt lgkmcnt(6)
	v_mfma_f32_32x32x16_bf16 v[160:175], v[2:5], v[184:187], v[160:175]
	s_waitcnt lgkmcnt(5)
	v_mfma_f32_32x32x16_bf16 v[144:159], v[8:11], v[184:187], v[144:159]
	s_waitcnt lgkmcnt(4)
	v_mfma_f32_32x32x16_bf16 v[160:175], v[208:211], v[188:191], v[160:175]
	s_waitcnt lgkmcnt(3)
	v_mfma_f32_32x32x16_bf16 v[144:159], v[244:247], v[188:191], v[144:159]
	ds_read_b128 v[244:247], v7 offset:8192
	s_nop 9
	v_exp_f32_e32 v6, v160
	v_exp_f32_e32 v3, v161
	v_exp_f32_e32 v10, v164
	v_exp_f32_e32 v11, v165
	v_exp_f32_e32 v160, v172
	v_exp_f32_e32 v161, v173
	v_exp_f32_e32 v5, v162
	v_exp_f32_e32 v2, v144
	v_exp_f32_e32 v7, v146
	v_exp_f32_e32 v144, v148
	v_exp_f32_e32 v146, v150
	v_exp_f32_e32 v148, v168
	v_exp_f32_e32 v150, v169
	v_exp_f32_e32 v4, v145
	v_exp_f32_e32 v145, v149
	v_exp_f32_e32 v12, v166
	v_exp_f32_e32 v149, v152
	v_exp_f32_e32 v152, v170
	v_exp_f32_e32 v162, v174
	v_exp_f32_e32 v8, v163
	v_exp_f32_e32 v9, v147
	v_exp_f32_e32 v13, v167
	v_exp_f32_e32 v147, v151
	v_exp_f32_e32 v151, v153
	v_exp_f32_e32 v153, v154
	v_exp_f32_e32 v154, v171
	v_exp_f32_e32 v163, v175
	v_exp_f32_e32 v156, v156
	v_exp_f32_e32 v157, v157
	v_add_f32_e32 v164, v6, v3
	v_add_f32_e32 v165, v10, v11
	v_add_f32_e32 v166, v148, v150
	v_add_f32_e32 v167, v160, v161
	v_exp_f32_e32 v158, v158
	v_add_f32_e32 v164, v5, v164
	v_add_f32_e32 v165, v12, v165
	v_add_f32_e32 v166, v152, v166
	v_add_f32_e32 v167, v162, v167
	v_exp_f32_e32 v155, v155
	v_exp_f32_e32 v159, v159
	v_add_f32_e32 v164, v8, v164
	v_add_f32_e32 v165, v13, v165
	v_add_f32_e32 v166, v154, v166
	v_add_f32_e32 v167, v163, v167
	v_add_f32_e32 v164, v2, v164
	v_add_f32_e32 v165, v144, v165
	v_add_f32_e32 v166, v149, v166
	v_add_f32_e32 v167, v156, v167
	v_add_f32_e32 v164, v4, v164
	v_add_f32_e32 v165, v145, v165
	v_add_f32_e32 v166, v151, v166
	v_add_f32_e32 v167, v157, v167
	v_add_f32_e32 v164, v7, v164
	v_add_f32_e32 v165, v146, v165
	v_add_f32_e32 v166, v153, v166
	v_add_f32_e32 v167, v158, v167
	v_add_f32_e32 v164, v9, v164
	v_add_f32_e32 v165, v147, v165
	v_add_f32_e32 v166, v155, v166
	v_add_f32_e32 v167, v159, v167
	v_add_f32_e32 v164, v164, v165
	v_add_f32_e32 v165, v166, v167
	v_add_f32_e32 v213, v164, v165
	v_mov_b32_e32 v218, v213
	v_cvt_pk_bf16_f32 v208, v6, v3
	v_cvt_pk_bf16_f32 v209, v5, v8
	v_cvt_pk_bf16_f32 v210, v10, v11
	v_cvt_pk_bf16_f32 v211, v12, v13
	v_cvt_pk_bf16_f32 v10, v148, v150
	v_cvt_pk_bf16_f32 v11, v152, v154
	v_cvt_pk_bf16_f32 v12, v160, v161
	v_cvt_pk_bf16_f32 v13, v162, v163
	v_cvt_pk_bf16_f32 v6, v2, v4
	v_cvt_pk_bf16_f32 v7, v7, v9
	v_cvt_pk_bf16_f32 v8, v144, v145
	v_cvt_pk_bf16_f32 v9, v146, v147
	v_cvt_pk_bf16_f32 v2, v149, v151
	v_cvt_pk_bf16_f32 v3, v153, v155
	v_cvt_pk_bf16_f32 v4, v156, v157
	v_cvt_pk_bf16_f32 v5, v158, v159
	v_permlane32_swap_b32_e32 v213, v218
	v_permlane32_swap_b32_e32 v208, v210
	v_permlane32_swap_b32_e32 v209, v211
	v_permlane32_swap_b32_e32 v10, v12
	v_permlane32_swap_b32_e32 v11, v13
	v_permlane32_swap_b32_e32 v6, v8
	v_permlane32_swap_b32_e32 v7, v9
	v_permlane32_swap_b32_e32 v2, v4
	v_permlane32_swap_b32_e32 v3, v5
	v_add_u32_e32 v252, s56, v224
	ds_read_b64_tr_b16 v[144:145], v252 offset:0x0
	ds_read_b64_tr_b16 v[146:147], v252 offset:0x800
	ds_read_b64_tr_b16 v[148:149], v252 offset:0x200
	ds_read_b64_tr_b16 v[150:151], v252 offset:0xa00
	ds_read_b64_tr_b16 v[152:153], v252 offset:0x400
	ds_read_b64_tr_b16 v[154:155], v252 offset:0xc00
	ds_read_b64_tr_b16 v[156:157], v252 offset:0x600
	ds_read_b64_tr_b16 v[158:159], v252 offset:0xe00
	s_waitcnt lgkmcnt(4)
	v_mfma_f32_32x32x16_bf16 v[112:127], v[208:211], v[144:147], v[112:127]
	v_mfma_f32_32x32x16_bf16 v[96:111], v[208:211], v[148:151], v[96:111]
	s_waitcnt lgkmcnt(0)
	v_mfma_f32_32x32x16_bf16 v[64:79], v[208:211], v[152:155], v[64:79]
	v_mfma_f32_32x32x16_bf16 v[48:63], v[208:211], v[156:159], v[48:63]
	v_mov_b32_e32 v160, 0
	s_andn2_b64 vcc, exec, s[44:45]
	v_mov_b32_e32 v161, 0
	v_mov_b32_e32 v162, 0
	v_mov_b32_e32 v163, 0
	v_mov_b32_e32 v164, 0
	v_mov_b32_e32 v165, 0
	v_mov_b32_e32 v166, 0
	v_mov_b32_e32 v167, 0
	v_mov_b32_e32 v168, 0
	v_mov_b32_e32 v169, 0
	v_mov_b32_e32 v170, 0
	v_mov_b32_e32 v171, 0
	v_mov_b32_e32 v172, 0
	v_mov_b32_e32 v173, 0
	v_mov_b32_e32 v174, 0
	v_mov_b32_e32 v175, 0
	v_mov_b32_e32 v144, 0
	v_mov_b32_e32 v145, 0
	v_mov_b32_e32 v146, 0
	v_mov_b32_e32 v147, 0
	v_mov_b32_e32 v148, 0
	v_mov_b32_e32 v149, 0
	v_mov_b32_e32 v150, 0
	v_mov_b32_e32 v151, 0
	v_mov_b32_e32 v152, 0
	v_mov_b32_e32 v153, 0
	v_mov_b32_e32 v154, 0
	v_mov_b32_e32 v155, 0
	v_mov_b32_e32 v156, 0
	v_mov_b32_e32 v157, 0
	v_mov_b32_e32 v158, 0
	v_mov_b32_e32 v159, 0
	s_cbranch_vccnz .LBB0_205
	s_andn2_b64 vcc, exec, s[42:43]
	s_mov_b64 s[42:43], -1
	s_cbranch_vccnz .LBB0_218
	v_add_u32_e32 v146, 0x21780, v219
	v_add_u32_e32 v147, 0x21708, v219
	v_add_u32_e32 v148, 0x21788, v219
	ds_read2_b32 v[144:145], v220 offset1:1
	ds_read2_b32 v[160:161], v146 offset1:1
	ds_read2_b32 v[146:147], v147 offset1:1
	ds_read2_b32 v[162:163], v148 offset1:1
	v_add_u32_e32 v148, 0x21720, v219
	v_add_u32_e32 v150, 0x217a0, v219
	v_add_u32_e32 v151, 0x21728, v219
	v_add_u32_e32 v152, 0x217a8, v219
	ds_read2_b32 v[148:149], v148 offset1:1
	ds_read2_b32 v[164:165], v150 offset1:1
	ds_read2_b32 v[150:151], v151 offset1:1
	ds_read2_b32 v[166:167], v152 offset1:1
	v_add_u32_e32 v152, 0x21740, v219
	v_add_u32_e32 v154, 0x217c0, v219
	v_add_u32_e32 v155, 0x21748, v219
	v_add_u32_e32 v156, 0x217c8, v219
	ds_read2_b32 v[152:153], v152 offset1:1
	ds_read2_b32 v[168:169], v154 offset1:1
	ds_read2_b32 v[154:155], v155 offset1:1
	ds_read2_b32 v[170:171], v156 offset1:1
	v_add_u32_e32 v156, 0x21760, v219
	v_add_u32_e32 v158, 0x217e0, v219
	v_add_u32_e32 v159, 0x21768, v219
	v_add_u32_e32 v174, 0x217e8, v219
	ds_read2_b32 v[156:157], v156 offset1:1
	ds_read2_b32 v[172:173], v158 offset1:1
	ds_read2_b32 v[158:159], v159 offset1:1
	ds_read2_b32 v[174:175], v174 offset1:1
	s_mov_b64 s[42:43], 0
